# top-k stagger by bit 3 of the workgroup id (half of every XCD's workgroups run the context unit first) instead of bit 0
# baseline (speedup 1.0000x reference)
.LBB0_1317:
	s_or_b64 exec, exec, s[4:5]
	v_readlane_b32 s6, v254, 26
	v_readlane_b32 s7, v254, 27
	s_and_b64 s[6:7], s[6:7], exec
	s_movk_i32 s1, 0x200
	s_mov_b64 s[4:5], s[96:97]
	s_waitcnt vmcnt(12)
	v_mov_b32_e32 v78, v0
	s_cselect_b32 s1, 0x100, s1
	s_mov_b32 s2, s80
	s_movk_i32 s100, 0x100
	s_bitcmp1_b32 s80, 3
	s_cbranch_scc0 .Lmy_tkf
	s_cmp_gt_u32 s1, 0x100
	s_cbranch_scc0 .Lmy_tkf
	s_add_i32 s2, s80, 0x100
	s_mov_b32 s100, 0xffffff00
